# speedup vs baseline: 1.0136x; 1.0136x over previous
_Z5k2_kvPKDF16_S0_S0_S0_PDF16_S1_Pf:
	s_load_dwordx8 s[12:19], s[0:1], 0x0
	s_lshl_b32 s3, s2, 1
	s_and_b32 s3, s3, 14
	s_bfe_u32 s25, s2, 0x10006
	v_bfe_u32 v4, v0, 6, 2
	v_and_b32_e32 v1, 15, v0
	s_or_b32 s5, s3, s25
	v_mul_u32_u24_e32 v4, 48, v4
	s_lshl_b32 s24, s5, 3
	s_movk_i32 s5, 0x100
	v_or_b32_e32 v47, v4, v1
	s_bfe_u32 s3, s2, 0x30003
	s_waitcnt lgkmcnt(0)
	v_mov_b32_e32 v2, s15
	v_mov_b32_e32 v3, s13
	v_cmp_gt_u32_e64 s[10:11], s5, v0
	v_mul_lo_u16_e32 v4, 57, v47
	s_lshl_b32 s26, s3, 4
	v_cndmask_b32_e64 v3, v2, v3, s[10:11]
	v_mov_b32_e32 v2, s14
	v_mov_b32_e32 v5, s12
	s_add_i32 s5, s24, -1
	v_lshrrev_b16_e32 v4, 10, v4
	v_cndmask_b32_e64 v2, v2, v5, s[10:11]
	s_add_i32 s6, s26, -1
	v_mul_i32_i24_e32 v5, 0xffffffee, v4
	v_add_u32_e32 v55, s5, v4
	s_lshr_b32 s4, s2, 7
	v_add3_u32 v57, s6, v47, v5
	v_max_i32_e32 v4, 0, v55
	v_mov_b32_e32 v6, 0x7f
	v_bfe_u32 v46, v0, 4, 2
	s_lshl_b32 s7, s4, 14
	v_med3_i32 v5, v57, 0, v6
	v_lshlrev_b32_e32 v4, 7, v4
	v_lshlrev_b32_e32 v48, 3, v46
	v_or3_b32 v4, v4, v5, s7
	v_lshl_or_b32 v42, v4, 6, v48
	v_mov_b32_e32 v43, 0
	v_lshl_add_u64 v[4:5], v[42:43], 1, v[2:3]
	v_add_u32_e32 v49, 16, v47
	v_mov_b32_e32 v7, 57
	global_load_dwordx4 v[18:21], v[4:5], off
	global_load_dwordx4 v[22:25], v[4:5], off offset:64
	v_mul_lo_u16_sdwa v4, v49, v7 dst_sel:DWORD dst_unused:UNUSED_PAD src0_sel:BYTE_0 src1_sel:DWORD
	v_lshrrev_b16_e32 v4, 10, v4
	v_mul_i32_i24_e32 v5, 0xffffffee, v4
	v_add_u32_e32 v74, s5, v4
	v_add3_u32 v75, s6, v49, v5
	v_med3_i32 v4, v74, 0, v6
	v_med3_i32 v5, v75, 0, v6
	v_lshlrev_b32_e32 v4, 7, v4
	v_or3_b32 v4, v4, v5, s7
	v_lshl_or_b32 v42, v4, 6, v48
	v_lshl_add_u64 v[4:5], v[42:43], 1, v[2:3]
	v_add_u32_e32 v51, 32, v47
	global_load_dwordx4 v[26:29], v[4:5], off
	global_load_dwordx4 v[30:33], v[4:5], off offset:64
	v_mul_lo_u16_sdwa v4, v51, v7 dst_sel:DWORD dst_unused:UNUSED_PAD src0_sel:BYTE_0 src1_sel:DWORD
	v_lshrrev_b16_e32 v4, 10, v4
	v_mul_i32_i24_e32 v5, 0xffffffee, v4
	v_add_u32_e32 v54, s5, v4
	v_add3_u32 v56, s6, v51, v5
	v_min_u32_e32 v4, 0x7f, v54
	v_med3_i32 v5, v56, 0, v6
	v_lshlrev_b32_e32 v4, 7, v4
	v_or3_b32 v4, v4, v5, s7
	v_lshl_or_b32 v42, v4, 6, v48
	v_lshl_add_u64 v[2:3], v[42:43], 1, v[2:3]
	global_load_dwordx4 v[34:37], v[2:3], off
	global_load_dwordx4 v[38:41], v[2:3], off offset:64
	v_lshrrev_b32_e32 v52, 8, v0
	v_lshlrev_b32_e32 v2, 7, v1
	v_lshl_or_b32 v42, v52, 14, v2
	v_lshl_add_u64 v[2:3], s[18:19], 0, v[42:43]
	v_lshlrev_b32_e32 v44, 4, v46
	v_mov_b32_e32 v45, v43
	v_lshl_add_u64 v[78:79], v[2:3], 0, v[44:45]
	v_bfe_u32 v45, v0, 7, 1
	v_bfe_u32 v50, v0, 6, 1
	s_lshl_b32 s5, s4, 6
	v_lshlrev_b32_e32 v3, 4, v45
	v_lshl_or_b32 v2, v50, 6, v48
	v_or3_b32 v10, v3, s5, v1
	s_lshl_b32 s5, s3, 5
	s_add_u32 s6, s16, s5
	v_lshrrev_b32_e32 v2, 4, v2
	v_mov_b32_e32 v11, v43
	s_addc_u32 s7, s17, 0
	v_and_b32_e32 v42, 16, v0
	v_or_b32_e32 v4, s24, v2
	v_lshlrev_b64 v[2:3], 15, v[10:11]
	v_or_b32_e32 v10, 32, v10
	v_lshl_add_u64 v[12:13], s[6:7], 0, v[42:43]
	v_lshlrev_b32_e32 v14, 8, v4
	v_lshlrev_b64 v[10:11], 15, v[10:11]
	s_mov_b64 s[28:29], 0x2000
	v_lshl_add_u64 v[78:79], v[78:79], 0, s[28:29]
	global_load_dwordx4 v[66:69], v[78:79], off
	global_load_dwordx4 v[70:73], v[78:79], off offset:64
	global_load_dwordx4 v[58:61], v[78:79], off offset:2048
	global_load_dwordx4 v[62:65], v[78:79], off offset:2112
	v_lshl_add_u64 v[2:3], v[12:13], 0, v[2:3]
	v_mov_b32_e32 v15, v43
	v_or_b32_e32 v16, 0x200, v14
	v_mov_b32_e32 v17, v43
	v_lshl_add_u64 v[10:11], v[12:13], 0, v[10:11]
	v_lshl_add_u64 v[4:5], v[2:3], 0, v[14:15]
	v_lshl_add_u64 v[6:7], v[2:3], 0, v[16:17]
	v_lshl_add_u64 v[12:13], v[10:11], 0, v[14:15]
	v_lshl_add_u64 v[14:15], v[10:11], 0, v[16:17]
	s_load_dwordx4 s[20:23], s[0:1], 0x20
	s_load_dwordx2 s[16:17], s[0:1], 0x30
	s_movk_i32 s0, 0x90
	v_lshrrev_b32_e32 v53, 6, v0
	s_mov_b32 s12, 0
	v_cmp_gt_u32_e32 vcc, s0, v0
	s_and_saveexec_b64 s[0:1], vcc
	s_cbranch_execz .LBB2_2
	v_lshlrev_b32_e32 v76, 4, v0
	v_mov_b32_e32 v77, v43
	v_lshl_add_u64 v[80:81], s[18:19], 0, v[76:77]
	v_add_co_u32_e32 v80, vcc, 0x8000, v80
	v_add_u32_e32 v76, 0x10e00, v76
	s_nop 0
	v_addc_co_u32_e32 v81, vcc, 0, v81, vcc
	global_load_dwordx4 v[80:83], v[80:81], off
	s_waitcnt vmcnt(0)
	ds_write_b128 v76, v[80:83]
.LBB2_2:
	s_or_b64 exec, exec, s[0:1]
	v_or_b32_e32 v55, v57, v55
	s_movk_i32 s0, 0x80
	v_cmp_gt_u32_e32 vcc, s0, v55
	v_or_b32_e32 v55, v75, v74
	s_movk_i32 s1, 0xb4
	s_waitcnt vmcnt(9)
	v_cndmask_b32_e32 v21, 0, v21, vcc
	v_cndmask_b32_e32 v20, 0, v20, vcc
	v_cndmask_b32_e32 v19, 0, v19, vcc
	v_cndmask_b32_e32 v18, 0, v18, vcc
	s_waitcnt vmcnt(8)
	v_cndmask_b32_e32 v25, 0, v25, vcc
	v_cndmask_b32_e32 v24, 0, v24, vcc
	v_cndmask_b32_e32 v23, 0, v23, vcc
	v_cndmask_b32_e32 v22, 0, v22, vcc
	v_cmp_gt_u32_e32 vcc, s0, v55
	v_or_b32_e32 v54, v56, v54
	v_lshrrev_b32_e32 v55, 2, v1
	s_waitcnt vmcnt(7)
	v_cndmask_b32_e32 v29, 0, v29, vcc
	v_cndmask_b32_e32 v28, 0, v28, vcc
	v_cndmask_b32_e32 v27, 0, v27, vcc
	v_cndmask_b32_e32 v26, 0, v26, vcc
	s_waitcnt vmcnt(6)
	v_cndmask_b32_e32 v33, 0, v33, vcc
	v_cndmask_b32_e32 v32, 0, v32, vcc
	v_cndmask_b32_e32 v31, 0, v31, vcc
	v_cndmask_b32_e32 v30, 0, v30, vcc
	v_cmp_gt_u32_e32 vcc, s1, v51
	v_cmp_gt_u32_e64 s[0:1], s0, v54
	s_and_b64 vcc, vcc, s[0:1]
	s_waitcnt vmcnt(5)
	v_cndmask_b32_e32 v37, 0, v37, vcc
	v_cndmask_b32_e32 v36, 0, v36, vcc
	v_cndmask_b32_e32 v35, 0, v35, vcc
	v_cndmask_b32_e32 v34, 0, v34, vcc
	s_waitcnt vmcnt(4)
	v_cndmask_b32_e32 v41, 0, v41, vcc
	v_cndmask_b32_e32 v40, 0, v40, vcc
	v_cndmask_b32_e32 v39, 0, v39, vcc
	v_cndmask_b32_e32 v38, 0, v38, vcc
	v_cmp_ne_u32_e32 vcc, 0, v42
	v_or_b32_e32 v75, v48, v55
	v_and_b32_e32 v56, 3, v0
	v_cndmask_b32_e64 v42, 0, 3, vcc
	v_add_u32_e32 v42, v42, v0
	v_and_b32_e32 v42, 15, v42
	v_mul_u32_u24_e32 v57, 0x3c00, v52
	v_mul_u32_u24_e32 v74, 0x2800, v52
	v_mul_u32_u24_e32 v75, 0x50, v75
	v_lshlrev_b32_e32 v76, 5, v45
	s_mov_b32 s5, s12
	s_movk_i32 s13, 0x50
	v_add3_u32 v74, v74, v75, v76
	v_lshlrev_b32_e32 v75, 3, v56
	v_or_b32_e32 v57, v57, v48
	v_mad_u32_u24 v48, v53, 18, v42
	s_lshl_b64 s[14:15], s[4:5], 14
	v_cmp_ne_u32_e64 s[4:5], 0, v56
	v_cmp_ne_u32_e64 s[6:7], 1, v56
	v_cmp_eq_u32_e64 s[8:9], 2, v56
	v_mul_u32_u24_e32 v56, 0x50, v49
	v_mov_b32_e32 v49, 0x5a0
	v_mad_u32_u24 v93, v48, s13, v49
	v_mov_b32_e32 v49, 0xa0
	v_mad_u32_u24 v92, v48, s13, v49
	v_mov_b32_e32 v49, 0x5f0
	v_mad_u32_u24 v94, v48, s13, v49
	v_mov_b32_e32 v49, 0x640
	v_mad_u32_u24 v95, v48, s13, v49
	v_mov_b32_e32 v49, 0xb40
	v_mad_u32_u24 v96, v48, s13, v49
	v_mov_b32_e32 v49, 0xb90
	s_movk_i32 s0, 0x7800
	s_movk_i32 s18, 0x2300
	v_lshlrev_b32_e32 v52, 12, v52
	v_mad_u32_u24 v97, v48, s13, v49
	v_mov_b32_e32 v49, 0xbe0
	v_lshl_or_b32 v54, v53, 4, v42
	v_add3_u32 v74, v74, v75, s0
	v_mov_b32_e32 v75, 0x7800
	v_lshlrev_b32_e32 v76, 8, v46
	v_mul_u32_u24_e32 v77, 0x50, v48
	v_mad_u32_u24 v91, v48, s13, s13
	v_mad_u32_u24 v98, v48, s13, v49
	v_mad_u32_u24 v48, v50, s18, v52
	v_lshlrev_b32_e32 v49, 10, v45
	v_mad_u32_u24 v54, v54, s13, v75
	v_mul_u32_u24_e32 v75, 0x2300, v50
	v_add3_u32 v48, v48, v49, v76
	v_lshlrev_b32_e32 v49, 2, v1
	v_lshlrev_b32_e32 v45, 6, v45
	v_cmp_eq_u32_e64 s[0:1], v55, v46
	v_and_b32_e32 v55, 0x100, v0
	v_or3_b32 v45, v75, v45, v49
	s_mov_b32 s13, 0xe900
	v_add3_u32 v84, v45, v55, s13
	v_add_u32_e32 v85, 0xe800, v45
	s_and_b32 s13, s2, 7
	v_lshlrev_b32_e32 v45, 7, v53
	v_lshl_or_b32 v45, s13, 11, v45
	v_lshl_or_b32 v45, s25, 10, v45
	v_or_b32_e32 v45, s14, v45
	v_or_b32_e32 v1, v48, v49
	v_mov_b32_e32 v49, s15
	v_or_b32_e32 v48, s26, v45
	v_lshl_add_u64 v[42:43], v[48:49], 0, v[42:43]
	v_lshlrev_b64 v[42:43], 7, v[42:43]
	s_mov_b32 s14, 0
	s_waitcnt lgkmcnt(0)
	s_barrier
	v_and_or_b32 v42, v0, 48, v42
	s_mov_b32 s15, 0
	v_mul_u32_u24_e32 v47, 0x50, v47
	v_mul_u32_u24_e32 v51, 0x50, v51
	v_mul_u32_u24_e32 v100, 0x1400, v50
	v_lshl_add_u64 v[42:43], v[42:43], 0, s[14:15]
	v_add_u32_e32 v1, 0xc800, v1
	s_waitcnt lgkmcnt(0)
	v_lshl_add_u64 v[80:81], s[22:23], 0, v[42:43]
	v_lshl_add_u64 v[82:83], s[20:21], 0, v[42:43]
	v_mul_u32_u24_e32 v86, 0x90, v46
	s_mov_b64 s[18:19], 0
	v_add_u32_e32 v87, v57, v47
	v_add_u32_e32 v88, v57, v56
	v_add_u32_e32 v89, v57, v51
	v_add_u32_e32 v90, v77, v44
	v_add_u32_e32 v91, v91, v44
	v_add_u32_e32 v92, v92, v44
	v_add_u32_e32 v93, v93, v44
	v_add_u32_e32 v94, v94, v44
	v_add_u32_e32 v95, v95, v44
	v_add_u32_e32 v96, v96, v44
	v_add_u32_e32 v97, v97, v44
	v_add_u32_e32 v98, v98, v44
	v_add_u32_e32 v99, v54, v44
	v_add_u32_e32 v100, v74, v100
	v_add_u32_e32 v1, 0xfffff000, v1
	v_add_u32_e32 v84, 0xffffff00, v84
	v_add_u32_e32 v85, 0xffffff00, v85
	v_add_u32_e32 v86, 0x480, v86
	s_mov_b32 s25, 2
	global_load_dwordx4 v[2:5], v[4:5], off
	s_nop 0
	global_load_dwordx4 v[6:9], v[6:7], off
	s_nop 0
	global_load_dwordx4 v[10:13], v[12:13], off
	s_nop 0
	global_load_dwordx4 v[14:17], v[14:15], off
	s_branch .LBB2_7
